# prep: transposed cross-lane reduction (2 permlane32 swaps, 1 permlane16 swap, 1 DPP add; 7 VALU instead of 28) and 4-byte LDS publishes; rest as v40
# speedup vs baseline: 1.0184x; 1.0108x over previous
_Z11prep_kernelPKfS0_S0_S0_Pf:
	s_load_dwordx8 s[4:11], s[0:1], 0x0
	s_load_dwordx2 s[12:13], s[0:1], 0x20
	s_cmpk_eq_i32 s2, 0x100
	s_cbranch_scc1 .Lprep_exit
	s_and_b32 s14, s2, 63
	s_lshr_b32 s15, s2, 6
	v_and_b32_e32 v1, 7, v0
	v_and_b32_e32 v2, 0x3f8, v0
	v_lshlrev_b32_e32 v3, 10, v2
	v_lshl_or_b32 v3, v1, 4, v3
	s_lshl_b32 s16, s15, 21
	s_lshl_b32 s17, s14, 7
	s_add_i32 s16, s16, s17
	v_add_u32_e32 v3, s16, v3
	v_add_u32_e32 v4, 0x100000, v3
	v_lshrrev_b32_e32 v5, 1, v2
	s_lshl_b32 s18, s15, 10
	v_add_u32_e32 v5, s18, v5
	v_and_b32_e32 v19, 63, v0
	v_lshrrev_b32_e32 v20, 6, v0
	v_and_b32_e32 v38, 7, v19
	v_lshlrev_b32_e32 v38, 4, v38
	v_lshrrev_b32_e32 v39, 4, v19
	v_lshl_add_u32 v38, v39, 2, v38
	v_lshl_add_u32 v38, v20, 7, v38
	v_and_b32_e32 v39, 8, v19
	s_waitcnt lgkmcnt(0)
	global_load_dwordx4 v[8:11], v3, s[4:5] nt
	global_load_dwordx4 v[12:15], v4, s[4:5] nt
	global_load_dword v6, v5, s[6:7]
	global_load_dword v16, v5, s[6:7] offset:512
	s_cmp_lt_u32 s14, 32
	s_cbranch_scc0 .Lprep_ld_done
	v_cmp_gt_u32_e32 vcc, 0x200, v0
	s_and_saveexec_b64 s[20:21], vcc
	s_cbranch_execz .Lprep_hb_skip
	v_lshrrev_b32_e32 v17, 5, v0
	v_and_b32_e32 v18, 31, v0
	v_lshlrev_b32_e32 v17, 12, v17
	v_lshl_or_b32 v17, v18, 2, v17
	v_add_u32_e32 v17, s17, v17
	global_load_dword v36, v17, s[10:11]

.Lprep_ld_done:
	s_getpc_b64 s[22:23]
	s_and_b32 s22, s22, 0xffffff00
	v_lshlrev_b32_e32 v25, 4, v0
	v_subrev_u32_e32 v30, 0x280, v0
	s_waitcnt vmcnt(0)
	v_pk_mul_f32 v[12:13], v[12:13], v[16:17] op_sel_hi:[1,0]
	v_pk_mul_f32 v[14:15], v[14:15], v[16:17] op_sel_hi:[1,0]
	v_pk_fma_f32 v[8:9], v[8:9], v[6:7], v[12:13] op_sel_hi:[1,0,1]
	v_pk_fma_f32 v[10:11], v[10:11], v[6:7], v[14:15] op_sel_hi:[1,0,1]
	s_nop 1
	v_permlane32_swap_b32_e32 v8, v10
	v_permlane32_swap_b32_e32 v9, v11
	v_add_f32_e32 v8, v8, v10
	v_add_f32_e32 v9, v9, v11
	s_nop 1
	v_permlane16_swap_b32_e32 v8, v9
	v_add_f32_e32 v8, v8, v9
	s_nop 1
	v_add_f32_dpp v8, v8, v8 row_ror:8 row_mask:0xf bank_mask:0xf bound_ctrl:1
	v_cmp_eq_u32_e32 vcc, 0, v39
	s_and_saveexec_b64 s[20:21], vcc
	ds_write_b32 v38, v8
	s_mov_b64 exec, s[20:21]
	s_cmp_lg_u32 s2, 0
	s_cbranch_scc1 .Lprep_bar
	v_mul_f32_e32 v23, v23, v24
	s_nop 1
	v_add_f32_dpp v23, v23, v23 quad_perm:[1,0,3,2] row_mask:0xf bank_mask:0xf bound_ctrl:1
	s_nop 1
	v_add_f32_dpp v23, v23, v23 quad_perm:[2,3,0,1] row_mask:0xf bank_mask:0xf bound_ctrl:1
	s_nop 1
	v_add_f32_dpp v23, v23, v23 row_ror:4 row_mask:0xf bank_mask:0xf bound_ctrl:1
	s_nop 1
	v_add_f32_dpp v23, v23, v23 row_ror:8 row_mask:0xf bank_mask:0xf bound_ctrl:1
	v_mov_b32_e32 v24, v23
	s_nop 1
	v_permlane16_swap_b32_e32 v23, v24
	v_add_f32_e32 v23, v23, v24
	v_mov_b32_e32 v24, v23
	s_nop 1
	v_permlane32_swap_b32_e32 v23, v24
	v_add_f32_e32 v23, v23, v24
	v_lshlrev_b32_e32 v22, 2, v20
	v_cmp_eq_u32_e32 vcc, 0, v19
	s_and_saveexec_b64 s[20:21], vcc
	ds_write_b32 v22, v23 offset:2048
	s_mov_b64 exec, s[20:21]
